# union6 + retC unit tail (XCD-local loop): 8 x global_store_dwordx2 per lane widened to 4 x dwordx4 with v_permlane32_swap pairs
# speedup vs baseline: 1.0043x; 1.0026x over previous
; #define GAS __attribute__((address_space(1)))
; #define WG_BAR() do { asm volatile("s_waitcnt vmcnt(0) lgkmcnt(0)" ::: "memory"); __builtin_amdgcn_s_barrier(); asm volatile("" ::: "memory"); } while (0)
; __device__ __forceinline__ unsigned pk2(float lo, float hi) { f32x2_t_ v = {lo, hi}; bf16x2_t_ b = __builtin_convertvector(v, bf16x2_t_); return __builtin_bit_cast(unsigned, b); }
; __device__ __forceinline__ void retC_unit(LAS unsigned char* lds, const bf16* proj, const f32x2* rot, const bf16* SST, bf16* Y, int u, int tid, int lane, int wid, Stopwatch& sw) {
;     ...
;     WG_BAR();
;     const float rs = 1.f / sqrtf((xs[il] + xs[128 + il]) * (1.f / 128.f) + NORM_EPS);
;     const bf16* gp = proj + (t0 + il) * LDP + C_GR + h * 128; bf16* yp = Y + (t0 + il) * LDY + 2048 + h * 128;
; #pragma unroll
;     for (int k = 0; k < 2; ++k)
; #pragma unroll
;         for (int r4 = 0; r4 < 4; ++r4) { const int e = 32 * (2 * eh + k) + 8 * r4 + 4 * hi; const v2u gw = gw_[k][r4];
;             v2u w; w.x = pk2(acc[k][4 * r4] * rs * bflo(gw.x), acc[k][4 * r4 + 1] * rs * bfhi(gw.x)); w.y = pk2(acc[k][4 * r4 + 2] * rs * bflo(gw.y), acc[k][4 * r4 + 3] * rs * bfhi(gw.y));
;             *(GAS v2u*)(yp + e) = w; }
.LBB0_633:
	s_or_b64 exec, exec, s[36:37]
	v_lshl_add_u32 v1, v130, 2, 0
	s_waitcnt vmcnt(0) lgkmcnt(0)
	s_barrier
	v_add_u32_e32 v1, 0x20000, v1
	ds_read2st64_b32 v[4:5], v1 offset1:2
	s_lshl_b32 s34, s0, 1
	s_waitcnt vmcnt(7)
	v_lshlrev_b32_e32 v10, 16, v112
	v_and_b32_e32 v11, 0xffff0000, v112
	v_lshlrev_b32_e32 v12, 16, v113
	s_waitcnt lgkmcnt(0)
	v_add_f32_e32 v1, v4, v5
	v_fmamk_f32 v1, v1, 0x3c000000, v240
	v_mul_f32_e32 v2, 0x4f800000, v1
	v_cmp_gt_f32_e32 vcc, s82, v1
	v_and_b32_e32 v13, 0xffff0000, v113
	s_movk_i32 s0, 0x1000
	v_cndmask_b32_e32 v1, v1, v2, vcc
	v_sqrt_f32_e32 v2, v1
	s_add_i32 s64, s64, s88
	v_readlane_b32 s50, v255, 22
	s_cmpk_lt_i32 s64, 0x400
	v_add_u32_e32 v4, -1, v2
	v_add_u32_e32 v5, 1, v2
	v_fma_f32 v6, -v4, v2, v1
	v_fma_f32 v7, -v5, v2, v1
	v_cmp_ge_f32_e64 s[36:37], 0, v6
	v_readlane_b32 s51, v255, 23
	s_nop 0
	v_cndmask_b32_e64 v2, v2, v4, s[36:37]
	v_cmp_lt_f32_e64 s[36:37], 0, v7
	s_nop 1
	v_cndmask_b32_e64 v2, v2, v5, s[36:37]
	v_mul_f32_e32 v4, 0x37800000, v2
	v_cndmask_b32_e32 v2, v2, v4, vcc
	v_cmp_class_f32_e32 vcc, v1, v241
	s_nop 1
	v_cndmask_b32_e32 v1, v2, v1, vcc
	v_div_scale_f32 v2, s[4:5], v1, v1, 1.0
	v_rcp_f32_e32 v4, v2
	v_readlane_b32 s4, v253, 61
	v_readlane_b32 s5, v253, 62
	v_fma_f32 v5, -v2, v4, 1.0
	v_fmac_f32_e32 v4, v5, v4
	v_div_scale_f32 v5, vcc, 1.0, v1, 1.0
	v_mul_f32_e32 v6, v5, v4
	v_fma_f32 v7, -v2, v6, v5
	v_fmac_f32_e32 v6, v7, v4
	v_fma_f32 v2, -v2, v6, v5
	v_div_fmas_f32 v2, v2, v4, v6
	v_mov_b64_e32 v[6:7], s[4:5]
	v_mad_u64_u32 v[6:7], s[4:5], v129, s67, v[6:7]
	v_div_fixup_f32 v4, v2, v1, 1.0
	v_mov_b32_e32 v2, v7
	v_mad_u64_u32 v[8:9], s[4:5], v128, s67, v[2:3]
	v_mov_b32_e32 v7, v8
	v_or_b32_e32 v1, s31, v132
	v_pk_mul_f32 v[8:9], v[34:35], v[4:5] op_sel_hi:[1,0]
	v_lshl_add_u64 v[6:7], v[6:7], 0, s[34:35]
	v_pk_mul_f32 v[8:9], v[8:9], v[10:11]
	v_pk_mul_f32 v[10:11], v[36:37], v[4:5] op_sel_hi:[1,0]
	v_lshlrev_b32_e32 v2, 1, v1
	v_pk_mul_f32 v[10:11], v[10:11], v[12:13]
	v_lshl_add_u64 v[6:7], v[6:7], 0, v[2:3]
	s_mov_b64 s[4:5], 0x1000
	v_cvt_pk_bf16_f32 v216, v8, v9
	v_cvt_pk_bf16_f32 v217, v10, v11
	v_lshl_add_u64 v[10:11], v[6:7], 0, s[4:5]
	v_lshlrev_b32_e32 v228, 1, v132
	v_mov_b32_e32 v229, 0
	v_lshl_add_u64 v[10:11], v[10:11], 0, v[228:229]
	v_add_co_u32_e32 v6, vcc, s0, v6
	s_waitcnt vmcnt(6)
	v_lshlrev_b32_e32 v12, 16, v111
	v_addc_co_u32_e32 v7, vcc, 0, v7, vcc
	v_pk_mul_f32 v[6:7], v[38:39], v[4:5] op_sel_hi:[1,0]
	v_lshlrev_b32_e32 v8, 16, v110
	v_and_b32_e32 v9, 0xffff0000, v110
	v_pk_mul_f32 v[6:7], v[6:7], v[8:9]
	v_pk_mul_f32 v[8:9], v[40:41], v[4:5] op_sel_hi:[1,0]
	v_and_b32_e32 v13, 0xffff0000, v111
	v_pk_mul_f32 v[8:9], v[8:9], v[12:13]
	v_cvt_pk_bf16_f32 v218, v6, v7
	v_cvt_pk_bf16_f32 v219, v8, v9
	s_nop 1
	v_permlane32_swap_b32 v216, v218
	v_permlane32_swap_b32 v217, v219
	global_store_dwordx4 v[10:11], v[216:219], off
	v_pk_mul_f32 v[6:7], v[42:43], v[4:5] op_sel_hi:[1,0]
	s_waitcnt vmcnt(7)
	v_lshlrev_b32_e32 v8, 16, v108
	v_and_b32_e32 v9, 0xffff0000, v108
	v_pk_mul_f32 v[6:7], v[6:7], v[8:9]
	v_pk_mul_f32 v[8:9], v[44:45], v[4:5] op_sel_hi:[1,0]
	v_lshlrev_b32_e32 v12, 16, v109
	v_and_b32_e32 v13, 0xffff0000, v109
	v_pk_mul_f32 v[8:9], v[8:9], v[12:13]
	v_cvt_pk_bf16_f32 v220, v6, v7
	v_cvt_pk_bf16_f32 v221, v8, v9
	v_pk_mul_f32 v[6:7], v[46:47], v[4:5] op_sel_hi:[1,0]
	s_waitcnt vmcnt(7)
	v_lshlrev_b32_e32 v8, 16, v106
	v_and_b32_e32 v9, 0xffff0000, v106
	v_pk_mul_f32 v[6:7], v[6:7], v[8:9]
	v_pk_mul_f32 v[8:9], v[48:49], v[4:5] op_sel_hi:[1,0]
	v_lshlrev_b32_e32 v12, 16, v107
	v_and_b32_e32 v13, 0xffff0000, v107
	v_pk_mul_f32 v[8:9], v[8:9], v[12:13]
	v_cvt_pk_bf16_f32 v222, v6, v7
	v_cvt_pk_bf16_f32 v223, v8, v9
	s_nop 1
	v_permlane32_swap_b32 v220, v222
	v_permlane32_swap_b32 v221, v223
	global_store_dwordx4 v[10:11], v[220:223], off offset:32
	v_pk_mul_f32 v[6:7], v[18:19], v[4:5] op_sel_hi:[1,0]
	s_waitcnt vmcnt(7)
	v_lshlrev_b32_e32 v8, 16, v104
	v_and_b32_e32 v9, 0xffff0000, v104
	v_pk_mul_f32 v[6:7], v[6:7], v[8:9]
	v_pk_mul_f32 v[8:9], v[20:21], v[4:5] op_sel_hi:[1,0]
	v_lshlrev_b32_e32 v12, 16, v105
	v_and_b32_e32 v13, 0xffff0000, v105
	v_pk_mul_f32 v[8:9], v[8:9], v[12:13]
	v_cvt_pk_bf16_f32 v216, v6, v7
	v_cvt_pk_bf16_f32 v217, v8, v9
	v_pk_mul_f32 v[6:7], v[22:23], v[4:5] op_sel_hi:[1,0]
	s_waitcnt vmcnt(7)
	v_lshlrev_b32_e32 v8, 16, v102
	v_and_b32_e32 v9, 0xffff0000, v102
	v_pk_mul_f32 v[6:7], v[6:7], v[8:9]
	v_pk_mul_f32 v[8:9], v[24:25], v[4:5] op_sel_hi:[1,0]
	v_lshlrev_b32_e32 v12, 16, v103
	v_and_b32_e32 v13, 0xffff0000, v103
	v_pk_mul_f32 v[8:9], v[8:9], v[12:13]
	v_cvt_pk_bf16_f32 v218, v6, v7
	v_cvt_pk_bf16_f32 v219, v8, v9
	s_nop 1
	v_permlane32_swap_b32 v216, v218
	v_permlane32_swap_b32 v217, v219
	global_store_dwordx4 v[10:11], v[216:219], off offset:64
	v_pk_mul_f32 v[6:7], v[26:27], v[4:5] op_sel_hi:[1,0]
	s_waitcnt vmcnt(7)
	v_lshlrev_b32_e32 v8, 16, v100
	v_and_b32_e32 v9, 0xffff0000, v100
	v_pk_mul_f32 v[6:7], v[6:7], v[8:9]
	v_pk_mul_f32 v[8:9], v[28:29], v[4:5] op_sel_hi:[1,0]
	v_lshlrev_b32_e32 v12, 16, v101
	v_and_b32_e32 v13, 0xffff0000, v101
	v_pk_mul_f32 v[8:9], v[8:9], v[12:13]
	v_cvt_pk_bf16_f32 v220, v6, v7
	v_cvt_pk_bf16_f32 v221, v8, v9
	v_pk_mul_f32 v[6:7], v[30:31], v[4:5] op_sel_hi:[1,0]
	s_waitcnt vmcnt(7)
	v_lshlrev_b32_e32 v8, 16, v98
	v_and_b32_e32 v9, 0xffff0000, v98
	v_pk_mul_f32 v[6:7], v[6:7], v[8:9]
	v_pk_mul_f32 v[4:5], v[32:33], v[4:5] op_sel_hi:[1,0]
	v_lshlrev_b32_e32 v8, 16, v99
	v_and_b32_e32 v9, 0xffff0000, v99
	v_pk_mul_f32 v[4:5], v[4:5], v[8:9]
	v_cvt_pk_bf16_f32 v222, v6, v7
	v_cvt_pk_bf16_f32 v223, v4, v5
	s_nop 1
	v_permlane32_swap_b32 v220, v222
	v_permlane32_swap_b32 v221, v223
	global_store_dwordx4 v[10:11], v[220:223], off offset:96
	s_waitcnt vmcnt(0) lgkmcnt(0)
	s_barrier
	s_cbranch_scc0 .LBB0_605
